# waves 1-7 touch the next phase's merge-gate bytes while waiting in the grid barrier before the merge GEMM (warms L2 / Infinity Cache; results discarded)
# baseline (speedup 1.0000x reference)
.LBB0_560:
	s_mul_i32 s0, s46, 10
	s_add_i32 s30, s0, 6
	v_readlane_b32 s0, v251, 10
	v_readlane_b32 s3, v251, 13
	s_cmp_lt_i32 s30, s3
	v_readlane_b32 s1, v251, 11
	v_readlane_b32 s2, v251, 12
	s_cbranch_scc0 .LBB0_573
	s_waitcnt vmcnt(0)
	s_waitcnt vmcnt(0) lgkmcnt(0)
	s_barrier
	v_readfirstlane_b32 s100, v0
	s_cmp_lt_u32 s100, 64
	s_cbranch_scc1 .Lpf5_skip
	v_readlane_b32 s4, v251, 4
	v_readlane_b32 s5, v251, 5
	v_readlane_b32 s8, v251, 0
	s_nop 3
	s_load_dwordx2 s[6:7], s[4:5], 0xc8
	v_lshrrev_b32_e32 v1, 1, v0
	v_and_b32_e32 v3, 1, v0
	v_lshlrev_b32_e32 v3, 7, v3
	s_movk_i32 s9, 0x2600
	v_mad_u32_u24 v1, v1, s9, v3
	s_and_b32 s10, s8, 7
	s_lshl_b32 s10, s10, 6
	s_lshr_b32 s11, s8, 3
	s_add_i32 s10, s10, s11
	s_lshr_b32 s11, s10, 5
	s_lshl_b32 s11, s11, 3
	s_and_b32 s100, s10, 7
	s_add_i32 s11, s11, s100
	s_bfe_u32 s100, s10, 0x20003
	s_mul_i32 s11, s11, 0x260000
	s_lshl_b32 s100, s100, 9
	s_add_i32 s11, s11, s100
	s_addk_i32 s11, 0x1600
	s_add_i32 s101, s11, 0x1300000
	v_add_u32_e32 v4, s11, v1
	v_add_u32_e32 v5, s101, v1
	s_waitcnt lgkmcnt(0)
	s_add_u32 s6, s6, 0x11400000
	s_addc_u32 s7, s7, 0
	global_load_dword v3, v4, s[6:7]
	global_load_dword v3, v4, s[6:7] offset:2048
	global_load_dword v3, v5, s[6:7]
	global_load_dword v3, v5, s[6:7] offset:2048
.Lpf5_skip:
	s_mov_b64 s[0:1], exec
	v_readlane_b32 s2, v252, 42
	v_readlane_b32 s3, v252, 43
	s_and_b64 s[2:3], s[0:1], s[2:3]
	v_readlane_b32 s47, v252, 56
	s_mov_b64 exec, s[2:3]
	s_cbranch_execz .LBB0_606
	v_readlane_b32 s2, v251, 8
	v_readlane_b32 s4, v252, 19
	v_readlane_b32 s3, v251, 9
	s_waitcnt vmcnt(0) expcnt(0) lgkmcnt(0)
	v_mov_b32_e32 v1, s4
	ds_read_b32 v6, v1
	v_readlane_b32 s4, v252, 20
	s_waitcnt lgkmcnt(0)
	v_cmp_ne_u32_e32 vcc, 0, v6
	v_mov_b32_e32 v1, s4
	ds_read_b32 v4, v1
	s_cbranch_vccnz .LBB0_577
	v_readlane_b32 s4, v251, 6
	v_readlane_b32 s5, v251, 7
	s_load_dwordx2 s[8:9], s[4:5], 0x4
	s_add_u32 s4, s2, 0x1000
	s_addc_u32 s5, s3, 0
	s_add_u32 s6, s2, 0x1100
	s_addc_u32 s7, s3, 0
	v_readlane_b32 s10, v251, 2
	s_waitcnt lgkmcnt(0)
	s_mul_i32 s31, s8, s10
	s_add_u32 s8, s2, 0x1200
	s_mul_i32 s31, s31, s9
	s_addc_u32 s9, s3, 0
	v_readlane_b32 s11, v251, 3
	s_add_u32 s10, s2, 0x1300
	s_addc_u32 s11, s3, 0
	s_mov_b32 s33, 1
	s_mov_b64 s[12:13], 0
	s_branch .LBB0_566
